# v38 + grid barrier between the gate/up GEMM and the down GEMM replaced by per-token-tile arrival counters
# speedup vs baseline: 1.0145x; 1.0145x over previous
; __device__ __forceinline__ unsigned xb_ld(unsigned* p)              { return __hip_atomic_load(p, __ATOMIC_RELAXED, __HIP_MEMORY_SCOPE_AGENT); }
; __device__ __forceinline__ unsigned xb_add(unsigned* p, unsigned v) { return __hip_atomic_fetch_add(p, v, __ATOMIC_RELAXED, __HIP_MEMORY_SCOPE_AGENT); }
; #define XB_SPIN(cond, bar) do { unsigned _sp = 0; while (cond) { __builtin_amdgcn_s_sleep(1); \
;     if ((++_sp & 255u) == 0u) { if (xb_ld(&(bar)[XB_TMO])) break; if (_sp > XB_SPIN_CAP) { atomicAdd(&(bar)[XB_TMO], 1u); break; } } } } while (0)
; __device__ __forceinline__ void xcd_barrier(const XcdBarrier& b) {
;     asm volatile("s_waitcnt vmcnt(0)" ::: "memory");
;     __syncthreads();
;     if (threadIdx.x == 0) {
;         unsigned* bar = b.bar;
;         __builtin_amdgcn_s_waitcnt(0);
;         unsigned nloc = b.st[0], nx = b.st[1];
;         if (nloc == 0u) { xcd_barrier_complete(bar, b.x, nloc, nx); b.st[0] = nloc; b.st[1] = nx; }
;         const unsigned old = xb_add(&bar[XB_XSUB(b.x)], 1u);
;         const unsigned gen = old / nloc;
;         if (old + 1u == (gen + 1u) * nloc) {
;             __builtin_amdgcn_fence(__ATOMIC_RELEASE, "agent");
;             asm volatile("s_waitcnt vmcnt(0)" ::: "memory");
;             const unsigned og = xb_add(&bar[XB_TOP], 1u);
;             const unsigned tg = og / nx;
;             if (og + 1u == (tg + 1u) * nx) xb_add(&bar[XB_TOPGEN], 1u);
;             else XB_SPIN(xb_ld(&bar[XB_TOPGEN]) == tg, bar);
;             __builtin_amdgcn_fence(__ATOMIC_ACQUIRE, "agent");
;             xb_add(&bar[XB_XGEN(b.x)], 1u);
;             asm volatile("s_waitcnt vmcnt(0)" ::: "memory");
;         } else {
;             XB_SPIN(xb_ld(&bar[XB_XGEN(b.x)]) == gen, bar);
;             __builtin_amdgcn_fence(__ATOMIC_ACQUIRE, "agent");
;             asm volatile("s_waitcnt vmcnt(0)" ::: "memory");
;         }
;     }
;     __syncthreads();
; }
.LBB0_599:
	v_readlane_b32 s0, v253, 42
	v_readlane_b32 s4, v253, 32
	s_add_i32 s0, s0, 1
	v_readlane_b32 s7, v253, 35
	s_cmp_ge_i32 s0, s7
	v_readlane_b32 s5, v253, 33
	v_readlane_b32 s6, v253, 34
	s_cbranch_scc1 .LBB0_645
	v_readlane_b32 s34, v253, 36
	v_readlane_b32 s35, v253, 37
	s_mov_b32 s1, s76
	s_waitcnt vmcnt(0)
	s_waitcnt vmcnt(0) lgkmcnt(0)
	s_barrier
	s_mov_b64 s[40:41], exec
	v_readlane_b32 s2, v253, 53
	v_readlane_b32 s3, v253, 54
	s_and_b64 s[2:3], s[40:41], s[2:3]
	s_mov_b64 exec, s[2:3]
	s_cbranch_execz .LBB0_644
	v_readlane_b32 s10, v253, 36
	v_readlane_b32 s11, v253, 37
	v_readlane_b32 s14, v253, 55
	s_nop 3
	s_add_u32 s12, s10, 0x5000
	s_addc_u32 s13, s11, 0
	s_and_b32 s15, s88, 7
	s_lshr_b32 s16, s88, 3
	s_lshl_b32 s15, s15, 3
	s_and_b32 s17, s16, 7
	s_add_i32 s17, s17, s15
	s_lshr_b32 s16, s16, 2
	s_add_i32 s16, s16, s15
	s_lshl_b32 s17, s17, 6
	s_lshl_b32 s16, s16, 6
	s_mov_b32 s16, s17
	s_add_i32 s14, s14, 1
	s_lshl_b32 s14, s14, 2
	v_mov_b32_e32 v2, s17
	v_mov_b32_e32 v5, 1
	v_mov_b32_e32 v4, s16
	global_atomic_add v2, v5, s[12:13]
	s_mov_b32 s18, 0
